# baseline (speedup 1.0000x reference)
.Lattn_noprio:
	s_lshl_b32 s12, s14, 11
	s_and_b32 s13, s13, 0x780
	s_or_b32 s12, s12, s13
	s_lshl_b32 s13, s24, 5
	s_add_i32 s12, s12, s13
	s_mul_hi_u32 s13, s12, 0x300
	s_mulk_i32 s12, 0x300
	s_lshl_b64 s[12:13], s[12:13], 1
	s_waitcnt lgkmcnt(0)
	s_add_u32 s4, s4, s12
	s_addc_u32 s5, s5, s13
	s_and_b32 s16, s3, 0xff
	s_lshl_b32 s3, s16, 6
	s_lshl_b32 s17, s16, 7
	s_add_u32 s18, s4, s17
	s_addc_u32 s19, s5, 0
	s_and_b32 s16, s15, 0x3fffffc0
	s_mul_i32 s14, s14, 0x300000
	s_add_u32 s4, s6, s14
	v_and_b32_e32 v212, 63, v0
	s_addc_u32 s5, s7, 0
	s_add_u32 s4, s4, s17
	v_mul_u32_u24_e32 v2, 0x300, v212
	s_addc_u32 s5, s5, 0
	v_lshlrev_b32_e32 v200, 1, v2
	v_mov_b32_e32 v201, 0
	s_lshl_b32 s20, s24, 4
	v_lshl_add_u64 v[2:3], s[4:5], 0, v[200:201]
	s_add_u32 s4, s8, s14
	s_addc_u32 s5, s9, 0
	s_mov_b32 s21, 0
	s_add_u32 s4, s4, s17
	v_lshl_add_u64 v[198:199], v[2:3], 0, s[20:21]
	s_addc_u32 s5, s5, 0
	v_bfe_u32 v2, v0, 2, 4
	s_lshr_b32 s6, s15, 2
	v_and_or_b32 v2, s6, 48, v2
	v_mul_u32_u24_e32 v2, 0x300, v2
	s_and_b32 s20, s6, 0x3fffffc0
	s_lshl_b32 s27, s24, 10
	v_lshlrev_b32_e32 v200, 1, v2
	s_cmp_lg_u32 0, -1
	v_lshl_add_u64 v[2:3], s[4:5], 0, v[200:201]
	v_lshlrev_b32_e32 v213, 3, v0
	s_cselect_b32 s4, 0, 0
	v_and_b32_e32 v50, 24, v213
	s_add_i32 s29, s27, s4
	s_mov_b32 s4, m0
	s_mov_b32 m0, s29
	s_nop 0
	global_load_lds_dwordx4 v[198:199], off
	s_mov_b32 m0, s4
	v_lshl_add_u64 v[2:3], v[2:3], 0, s[20:21]
	v_lshlrev_b32_e32 v200, 1, v50
	v_lshl_add_u64 v[194:195], v[198:199], 0, 64
	s_add_i32 s28, s29, 0x1000
	s_mov_b32 s4, m0
	s_mov_b32 m0, s28
	s_nop 0
	global_load_lds_dwordx4 v[194:195], off
	s_mov_b32 m0, s4
	v_lshl_add_u64 v[202:203], v[2:3], 0, v[200:201]
	s_add_i32 s26, s29, 0x6000
	s_mov_b32 s4, m0
	s_mov_b32 m0, s26
	s_nop 0
	global_load_lds_dwordx4 v[202:203], off
	s_mov_b32 m0, s4
	v_lshl_add_u64 v[196:197], v[202:203], 0, 64
	s_add_i32 s25, s29, 0x7000
	s_mov_b32 s4, m0
	s_mov_b32 m0, s25
	s_nop 0
	global_load_lds_dwordx4 v[196:197], off
	s_mov_b32 m0, s4
	s_mov_b64 s[4:5], 0x18000
	v_lshl_add_u64 v[2:3], v[198:199], 0, s[4:5]
	s_mov_b64 s[14:15], 0x18040
	v_and_b32_e32 v214, 31, v0
	v_bfe_u32 v215, v0, 5, 1
	s_add_i32 s6, s29, 0x2000
	s_mov_b32 s7, m0
	s_mov_b32 m0, s6
	s_nop 0
	global_load_lds_dwordx4 v[2:3], off
	s_mov_b32 m0, s7
	v_lshl_add_u64 v[2:3], v[198:199], 0, s[14:15]
	s_add_i32 s6, s29, 0x3000
	s_mov_b32 s7, m0
	s_mov_b32 m0, s6
	s_nop 0
	global_load_lds_dwordx4 v[2:3], off
	s_mov_b32 m0, s7
	v_mul_u32_u24_e32 v2, 0x300, v214
	v_lshlrev_b32_e32 v200, 4, v215
	v_lshl_or_b32 v2, v2, 1, v200
	global_load_dwordx4 v[174:177], v2, s[18:19]
	global_load_dwordx4 v[170:173], v2, s[18:19] offset:32
	global_load_dwordx4 v[166:169], v2, s[18:19] offset:64
	global_load_dwordx4 v[162:165], v2, s[18:19] offset:96
	s_mov_b64 s[6:7], 0x30000
	s_mov_b64 s[8:9], 0x30040
	v_lshlrev_b32_e32 v2, 10, v215
	v_lshlrev_b32_e32 v3, 4, v214
	v_add3_u32 v218, 0, v2, v3
	v_lshl_add_u64 v[2:3], v[198:199], 0, s[6:7]
	v_lshl_add_u64 v[4:5], v[198:199], 0, s[8:9]
	s_add_i32 s8, s29, 0x4000
	s_mov_b32 s17, m0
	s_mov_b32 m0, s8
	s_nop 0
	global_load_lds_dwordx4 v[2:3], off
	s_mov_b32 m0, s17
	s_add_i32 s9, s29, 0x5000
	s_mov_b32 s8, m0
	s_mov_b32 m0, s9
	s_nop 0
	global_load_lds_dwordx4 v[4:5], off
	s_mov_b32 m0, s8
	s_waitcnt vmcnt(6) lgkmcnt(0)
	s_barrier
	ds_read_b128 v[2:5], v218
	ds_read_b128 v[6:9], v218 offset:512
	ds_read_b128 v[34:37], v218 offset:2048
	ds_read_b128 v[38:41], v218 offset:2560
	s_mov_b64 s[8:9], 0x48000
	s_mov_b64 s[18:19], 0x48040
	s_mov_b32 s31, -1
	s_movk_i32 s35, 0x2000
	s_movk_i32 s33, 0x4000
	s_mov_b32 s34, 0x41000000
	s_waitcnt vmcnt(3) lgkmcnt(3)
	v_mfma_f32_32x32x16_f16 v[18:33], v[2:5], v[174:177], 0
	s_waitcnt lgkmcnt(2)
	v_mfma_f32_32x32x16_f16 v[2:17], v[6:9], v[174:177], 0
	s_waitcnt vmcnt(2) lgkmcnt(1)
	v_mfma_f32_32x32x16_f16 v[18:33], v[34:37], v[170:173], v[18:33]
	s_waitcnt lgkmcnt(0)
	v_mfma_f32_32x32x16_f16 v[2:17], v[38:41], v[170:173], v[2:17]
	ds_read_b128 v[34:37], v218 offset:4096
	ds_read_b128 v[38:41], v218 offset:4608
	s_waitcnt vmcnt(1) lgkmcnt(1)
	v_mfma_f32_32x32x16_f16 v[18:33], v[34:37], v[166:169], v[18:33]
	s_waitcnt lgkmcnt(0)
	v_mfma_f32_32x32x16_f16 v[2:17], v[38:41], v[166:169], v[2:17]
	ds_read_b128 v[34:37], v218 offset:6144
	ds_read_b128 v[38:41], v218 offset:6656
	s_waitcnt vmcnt(0) lgkmcnt(1)
	v_mfma_f32_32x32x16_f16 v[18:33], v[34:37], v[162:165], v[18:33]
	s_waitcnt lgkmcnt(0)
	v_mfma_f32_32x32x16_f16 v[2:17], v[38:41], v[162:165], v[2:17]
	s_nop 9
	v_max_f32_e32 v34, v19, v19
	v_max_f32_e32 v35, v18, v18
	v_max_f32_e32 v34, v35, v34
	v_max3_f32 v36, v20, v21, v3
	v_max3_f32 v34, v34, v2, v4
	v_max3_f32 v35, v36, v24, v25
	v_max3_f32 v34, v34, v5, v22
	v_max3_f32 v35, v35, v8, v9
	v_max3_f32 v34, v34, v23, v6
	v_max3_f32 v35, v35, v28, v29
	v_max3_f32 v34, v34, v7, v26
	v_max3_f32 v35, v35, v12, v13
	v_max3_f32 v34, v34, v27, v10
	v_max3_f32 v35, v35, v32, v33
	v_max3_f32 v34, v34, v11, v30
	v_max3_f32 v35, v35, v16, v17
	v_max3_f32 v34, v34, v31, v14
	v_max3_f32 v34, v34, v15, v35
	v_mov_b32_e32 v35, v34
	s_nop 1
	v_permlane32_swap_b32_e32 v34, v35
	v_max_f32_e32 v35, v35, v35
	v_max_f32_e32 v34, v34, v34
	v_max_f32_e32 v219, v34, v35
	v_xor_b32_e32 v34, 0x80000000, v219
	v_mov_b32_e32 v35, v34
	v_mov_b32_e32 v36, v34
	v_mov_b32_e32 v37, v34
	v_mov_b32_e32 v38, v34
	v_mov_b32_e32 v39, v34
	v_mov_b32_e32 v40, v34
	v_mov_b32_e32 v41, v34
	v_mov_b32_e32 v42, v34
	v_mov_b32_e32 v43, v34
	v_mov_b32_e32 v44, v34
	v_mov_b32_e32 v45, v34
	v_mov_b32_e32 v46, v34
	v_mov_b32_e32 v47, v34
	v_mov_b32_e32 v48, v34
	v_mov_b32_e32 v49, v34
	s_waitcnt vmcnt(0) lgkmcnt(0)
	s_barrier
	v_sub_f32_e32 v51, v2, v219
	v_sub_f32_e32 v52, v3, v219
	v_lshl_add_u64 v[2:3], v[198:199], 0, s[8:9]
	s_mov_b32 s17, m0
	s_mov_b32 m0, s29
	s_nop 0
	global_load_lds_dwordx4 v[2:3], off
	s_mov_b32 m0, s17
	v_lshl_add_u64 v[2:3], v[198:199], 0, s[18:19]
	s_mov_b32 s17, m0
	s_mov_b32 m0, s28
	s_nop 0
	global_load_lds_dwordx4 v[2:3], off
	s_mov_b32 m0, s17
	s_add_i32 s17, s29, 0x8000
	v_lshl_add_u64 v[2:3], v[202:203], 0, s[4:5]
	s_mov_b32 s4, m0
	s_mov_b32 m0, s17
	s_nop 0
	global_load_lds_dwordx4 v[2:3], off
	s_mov_b32 m0, s4
	s_add_i32 s4, s29, 0x9000
	v_lshl_add_u64 v[2:3], v[202:203], 0, s[14:15]
	s_mov_b32 s5, m0
	s_mov_b32 m0, s4
	s_nop 0
	global_load_lds_dwordx4 v[2:3], off
	s_mov_b32 m0, s5
	ds_read_b128 v[82:85], v218 offset:8192
	ds_read_b128 v[182:185], v218 offset:8704
	ds_read_b128 v[178:181], v218 offset:10240
	ds_read_b128 v[142:145], v218 offset:10752
	ds_read_b128 v[138:141], v218 offset:12288
	ds_read_b128 v[134:137], v218 offset:12800
	ds_read_b128 v[130:133], v218 offset:14336
	ds_read_b128 v[126:129], v218 offset:14848
	v_lshlrev_b32_e32 v2, 1, v0
	v_and_b32_e32 v2, 32, v2
	v_sub_f32_e32 v18, v18, v219
	v_sub_f32_e32 v19, v19, v219
	v_sub_f32_e32 v20, v20, v219
	v_sub_f32_e32 v21, v21, v219
	v_sub_f32_e32 v22, v22, v219
	v_sub_f32_e32 v23, v23, v219
	v_sub_f32_e32 v24, v24, v219
	v_sub_f32_e32 v25, v25, v219
	v_sub_f32_e32 v26, v26, v219
	v_sub_f32_e32 v27, v27, v219
	v_sub_f32_e32 v28, v28, v219
	v_sub_f32_e32 v29, v29, v219
	v_sub_f32_e32 v30, v30, v219
	v_sub_f32_e32 v31, v31, v219
	v_sub_f32_e32 v32, v32, v219
	v_sub_f32_e32 v33, v33, v219
	v_sub_f32_e32 v4, v4, v219
	v_sub_f32_e32 v5, v5, v219
	v_sub_f32_e32 v6, v6, v219
	v_sub_f32_e32 v7, v7, v219
	v_sub_f32_e32 v8, v8, v219
	v_sub_f32_e32 v9, v9, v219
	v_sub_f32_e32 v10, v10, v219
	v_sub_f32_e32 v11, v11, v219
	v_sub_f32_e32 v12, v12, v219
	v_sub_f32_e32 v13, v13, v219
	v_sub_f32_e32 v14, v14, v219
	v_sub_f32_e32 v15, v15, v219
	v_sub_f32_e32 v16, v16, v219
	v_sub_f32_e32 v17, v17, v219
	v_add3_u32 v2, 0, v2, v50
	v_lshlrev_b32_e32 v3, 8, v215
	v_and_b32_e32 v50, 0xc0, v1
	v_add3_u32 v216, v2, v3, v50
	v_exp_f32_e32 v66, v18
	v_exp_f32_e32 v67, v19
	v_exp_f32_e32 v50, v51
	v_exp_f32_e32 v51, v52
	v_exp_f32_e32 v68, v20
	v_exp_f32_e32 v52, v4
	v_exp_f32_e32 v69, v21
	v_exp_f32_e32 v53, v5
	v_exp_f32_e32 v70, v22
	v_exp_f32_e32 v54, v6
	v_exp_f32_e32 v71, v23
	v_exp_f32_e32 v55, v7
	v_exp_f32_e32 v72, v24
	v_exp_f32_e32 v56, v8
	v_exp_f32_e32 v73, v25
	v_exp_f32_e32 v57, v9
	v_exp_f32_e32 v74, v26
	v_exp_f32_e32 v58, v10
	v_exp_f32_e32 v75, v27
	v_exp_f32_e32 v59, v11
	v_exp_f32_e32 v76, v28
	v_exp_f32_e32 v60, v12
	v_exp_f32_e32 v77, v29
	v_exp_f32_e32 v61, v13
	v_exp_f32_e32 v78, v30
	v_exp_f32_e32 v62, v14
	v_exp_f32_e32 v79, v31
	v_exp_f32_e32 v63, v15
	v_exp_f32_e32 v80, v32
	v_exp_f32_e32 v64, v16
	v_exp_f32_e32 v81, v33
	v_exp_f32_e32 v65, v17
	s_lshl_b32 s4, s16, 2
	s_waitcnt vmcnt(4) lgkmcnt(0)
	s_barrier
	s_add_i32 s30, s4, 0
	v_cmp_gt_u32_e64 s[4:5], 32, v212
	s_mov_b64 s[14:15], 0
	s_mov_b64 s[16:17], 0x60000
	s_mov_b64 s[18:19], 0x78000
	v_mov_b32_e32 v2, v201
	v_mov_b32_e32 v3, v201
	v_mov_b32_e32 v4, v201
	v_mov_b32_e32 v5, v201
	v_mov_b32_e32 v6, v201
	v_mov_b32_e32 v7, v201
	v_mov_b32_e32 v8, v201
	v_mov_b32_e32 v9, v201
	v_mov_b32_e32 v10, v201
	v_mov_b32_e32 v11, v201
	v_mov_b32_e32 v12, v201
	v_mov_b32_e32 v13, v201
	v_mov_b32_e32 v14, v201
	v_mov_b32_e32 v15, v201
	v_mov_b32_e32 v16, v201
	v_mov_b32_e32 v17, v201
	v_mov_b32_e32 v18, v201
	v_mov_b32_e32 v19, v201
	v_mov_b32_e32 v20, v201
	v_mov_b32_e32 v21, v201
	v_mov_b32_e32 v22, v201
	v_mov_b32_e32 v23, v201
	v_mov_b32_e32 v24, v201
	v_mov_b32_e32 v25, v201
	v_mov_b32_e32 v26, v201
	v_mov_b32_e32 v27, v201
	v_mov_b32_e32 v28, v201
	v_mov_b32_e32 v29, v201
	v_mov_b32_e32 v30, v201
	v_mov_b32_e32 v31, v201
	v_mov_b32_e32 v32, v201
	v_mov_b32_e32 v33, v201
	v_lshl_add_u32 v217, v214, 2, s30
	v_readfirstlane_b32 s40, v198
	v_readfirstlane_b32 s41, v199
	v_readfirstlane_b32 s42, v202
	v_readfirstlane_b32 s43, v203
	s_nop 3
	v_subrev_u32_e32 v221, s40, v198
	v_subrev_u32_e32 v222, s42, v202
	s_add_u32 s44, s40, s16
	s_addc_u32 s45, s41, s17
	s_add_u32 s46, s44, 64
	s_addc_u32 s47, s45, 0
	s_add_u32 s48, s42, s6
	s_addc_u32 s49, s43, s7
	s_add_u32 s50, s48, 64
	s_addc_u32 s51, s49, 0
	s_add_u32 s52, s40, s18
	s_addc_u32 s53, s41, s19
	s_add_u32 s54, s52, 64
	s_addc_u32 s55, s53, 0
	s_add_u32 s56, s42, s8
	s_addc_u32 s57, s43, s9
	s_add_u32 s58, s56, 64
	s_addc_u32 s59, s57, 0
